# baseline (speedup 1.0000x reference)
.LBB1_31:
	s_or_b64 exec, exec, s[18:19]
	s_waitcnt lgkmcnt(0)
	s_barrier
	s_mov_b32 s40, 0xc350
	s_movk_i32 s41, 0xc40
	v_lshlrev_b32_e32 v48, 3, v0
	v_and_b32_e32 v48, 0x78, v48
	v_mov_b32_e32 v49, 0
	v_lshl_add_u64 v[48:49], s[34:35], 0, v[48:49]
	v_lshlrev_b32_e32 v50, 2, v25
	v_cmp_gt_i32_e64 s[44:45], s40, v28
	s_and_saveexec_b64 s[42:43], s[44:45]
	ds_read_b32 v51, v50 offset:19456
	v_mov_b32_e32 v52, v28
	v_mov_b32_e32 v53, 0
	v_lshlrev_b64 v[52:53], 7, v[52:53]
	s_waitcnt lgkmcnt(0)
	v_mul_f32_e32 v14, v51, v14
	v_mul_f32_e32 v15, v51, v15
	v_mul_f32_e32 v16, v51, v16
	v_mul_f32_e32 v17, v51, v17
	v_cvt_pk_f16_f32 v14, v14, v15
	v_cvt_pk_f16_f32 v15, v16, v17
	v_lshl_add_u64 v[52:53], v[48:49], 0, v[52:53]
	global_store_dwordx2 v[52:53], v[14:15], off sc0 sc1
	s_or_b64 exec, exec, s[42:43]
	v_cmp_gt_i32_e64 s[44:45], s40, v26
	s_and_saveexec_b64 s[42:43], s[44:45]
	ds_read_b32 v51, v50 offset:19712
	v_mov_b32_e32 v52, v26
	v_mov_b32_e32 v53, 0
	v_lshlrev_b64 v[52:53], 7, v[52:53]
	s_waitcnt lgkmcnt(0)
	v_mul_f32_e32 v10, v51, v10
	v_mul_f32_e32 v11, v51, v11
	v_mul_f32_e32 v12, v51, v12
	v_mul_f32_e32 v13, v51, v13
	v_cvt_pk_f16_f32 v10, v10, v11
	v_cvt_pk_f16_f32 v11, v12, v13
	v_lshl_add_u64 v[52:53], v[48:49], 0, v[52:53]
	global_store_dwordx2 v[52:53], v[10:11], off sc0 sc1
	s_or_b64 exec, exec, s[42:43]
	v_cmp_gt_i32_e64 s[44:45], s40, v24
	s_and_saveexec_b64 s[42:43], s[44:45]
	ds_read_b32 v51, v50 offset:19968
	v_mov_b32_e32 v52, v24
	v_mov_b32_e32 v53, 0
	v_lshlrev_b64 v[52:53], 7, v[52:53]
	s_waitcnt lgkmcnt(0)
	v_mul_f32_e32 v6, v51, v6
	v_mul_f32_e32 v7, v51, v7
	v_mul_f32_e32 v8, v51, v8
	v_mul_f32_e32 v9, v51, v9
	v_cvt_pk_f16_f32 v6, v6, v7
	v_cvt_pk_f16_f32 v7, v8, v9
	v_lshl_add_u64 v[52:53], v[48:49], 0, v[52:53]
	global_store_dwordx2 v[52:53], v[6:7], off sc0 sc1
	s_or_b64 exec, exec, s[42:43]
	v_cmp_gt_u32_e64 s[44:45], s41, v32
	v_cmp_gt_i32_e64 s[46:47], s40, v22
	s_and_b64 s[44:45], s[44:45], s[46:47]
	v_lshlrev_b32_e32 v54, 2, v23
	s_and_saveexec_b64 s[42:43], s[44:45]
	ds_read_b32 v51, v54 offset:19456
	v_mov_b32_e32 v52, v22
	v_mov_b32_e32 v53, 0
	v_lshlrev_b64 v[52:53], 7, v[52:53]
	s_waitcnt lgkmcnt(0)
	v_mul_f32_e32 v2, v51, v2
	v_mul_f32_e32 v3, v51, v3
	v_mul_f32_e32 v4, v51, v4
	v_mul_f32_e32 v5, v51, v5
	v_cvt_pk_f16_f32 v2, v2, v3
	v_cvt_pk_f16_f32 v3, v4, v5
	v_lshl_add_u64 v[52:53], v[48:49], 0, v[52:53]
	global_store_dwordx2 v[52:53], v[2:3], off sc0 sc1
	s_or_b64 exec, exec, s[42:43]
	s_and_saveexec_b64 s[30:31], s[8:9]
	s_cbranch_execz .LBB1_38
	v_lshrrev_b32_e32 v18, 6, v0
	v_cmp_gt_u32_e64 s[8:9], 49, v38
	v_mov_b32_e32 v19, -1
	s_and_saveexec_b64 s[12:13], s[8:9]
	s_cbranch_execz .LBB1_34
	v_mad_u32_u24 v19, v18, 49, v38
	v_lshlrev_b32_e32 v39, 2, v19
	ds_read_b32 v39, v39 offset:16384
	s_waitcnt lgkmcnt(0)
	v_lshl_or_b32 v19, v39, 8, v19
